# l3sleep3
# baseline (speedup 1.0000x reference)
.LBB1_3:
	s_and_b32 s8, s55, 6
	ds_read_b128 v[114:117], v77
	ds_read_b128 v[118:121], v77 offset:512
	ds_read_b128 v[122:125], v77 offset:1024
	ds_read_b128 v[126:129], v77 offset:1536
	ds_read_b64 v[90:91], v78
	ds_read_b64 v[92:93], v78 offset:8
	ds_read_b64 v[94:95], v78 offset:16
	ds_read_b64 v[96:97], v81
	ds_read_b64 v[98:99], v81 offset:8
	ds_read_b64 v[100:101], v81 offset:16
	v_lshl_add_u32 v89, s8, 9, v87
	ds_read_u16 v154, v89
	ds_read_b128 v[130:133], v77 offset:8192
	ds_read_b128 v[134:137], v77 offset:8704
	ds_read_b128 v[138:141], v77 offset:9216
	ds_read_b128 v[142:145], v77 offset:9728
	ds_read_b64 v[102:103], v80
	ds_read_b64 v[104:105], v80 offset:8
	ds_read_b64 v[106:107], v80 offset:16
	s_mov_b32 m0, s50
	ds_read_b64 v[108:109], v79
	ds_read_b64 v[110:111], v79 offset:8
	ds_read_b64 v[112:113], v79 offset:16
	ds_read_u16 v89, v89 offset:512
	global_load_lds_dwordx4 v161, s[72:73]
	s_mov_b32 m0, s51
	s_add_i32 s56, s37, s55
	global_load_lds_dwordx4 v162, s[72:73]
	s_mov_b32 m0, s52
	s_add_i32 s8, s56, 4
	global_load_lds_dwordx4 v167, s[76:77]
	s_mov_b32 m0, s53
	s_min_u32 s57, s8, 63
	global_load_lds_dwordx4 v168, s[76:77]
	s_mov_b32 m0, s54
	s_lshl_b32 s8, s57, 10
	global_load_lds_dwordx4 v169, s[76:77]
	s_add_u32 s82, s80, s8
	s_addc_u32 s83, s81, 0
	s_lshl_b32 s8, s57, 9
	s_and_b32 s8, s8, 0xe00
	s_add_i32 m0, s49, s8
	s_add_i32 s57, s55, 4
	global_load_lds_dword v160, s[82:83]
	s_sleep 3
	s_waitcnt vmcnt(6)
	s_waitcnt lgkmcnt(0)
	s_barrier
	s_setprio 1
	s_waitcnt lgkmcnt(0)
	v_mfma_scale_f32_32x32x64_f8f6f4 v[50:65], v[90:95], v[114:117], v[50:65], v154, v88 op_sel_hi:[0,0,0] cbsz:2 blgp:4
	v_mfma_scale_f32_32x32x64_f8f6f4 v[34:49], v[90:95], v[118:121], v[34:49], v154, v88 op_sel_hi:[0,0,0] cbsz:2 blgp:4
	v_mfma_scale_f32_32x32x64_f8f6f4 v[18:33], v[90:95], v[122:125], v[18:33], v154, v88 op_sel_hi:[0,0,0] cbsz:2 blgp:4
	v_mfma_scale_f32_32x32x64_f8f6f4 v[2:17], v[90:95], v[126:129], v[2:17], v154, v88 op_sel_hi:[0,0,0] cbsz:2 blgp:4
	v_mfma_scale_f32_32x32x64_f8f6f4 v[50:65], v[96:101], v[114:117], v[50:65], v154, v88 op_sel:[1,0,0] op_sel_hi:[0,0,0] cbsz:2 blgp:4
	v_mfma_scale_f32_32x32x64_f8f6f4 v[34:49], v[96:101], v[118:121], v[34:49], v154, v88 op_sel:[1,0,0] op_sel_hi:[0,0,0] cbsz:2 blgp:4
	v_mfma_scale_f32_32x32x64_f8f6f4 v[18:33], v[96:101], v[122:125], v[18:33], v154, v88 op_sel:[1,0,0] op_sel_hi:[0,0,0] cbsz:2 blgp:4
	v_mfma_scale_f32_32x32x64_f8f6f4 v[2:17], v[96:101], v[126:129], v[2:17], v154, v88 op_sel:[1,0,0] op_sel_hi:[0,0,0] cbsz:2 blgp:4
	v_mfma_scale_f32_32x32x64_f8f6f4 v[50:65], v[102:107], v[130:133], v[50:65], v89, v88 op_sel_hi:[0,0,0] cbsz:2 blgp:4
	v_mfma_scale_f32_32x32x64_f8f6f4 v[34:49], v[102:107], v[134:137], v[34:49], v89, v88 op_sel_hi:[0,0,0] cbsz:2 blgp:4
	v_mfma_scale_f32_32x32x64_f8f6f4 v[18:33], v[102:107], v[138:141], v[18:33], v89, v88 op_sel_hi:[0,0,0] cbsz:2 blgp:4
	v_mfma_scale_f32_32x32x64_f8f6f4 v[2:17], v[102:107], v[142:145], v[2:17], v89, v88 op_sel_hi:[0,0,0] cbsz:2 blgp:4
	v_mfma_scale_f32_32x32x64_f8f6f4 v[50:65], v[108:113], v[130:133], v[50:65], v89, v88 op_sel:[1,0,0] op_sel_hi:[0,0,0] cbsz:2 blgp:4
	v_mfma_scale_f32_32x32x64_f8f6f4 v[34:49], v[108:113], v[134:137], v[34:49], v89, v88 op_sel:[1,0,0] op_sel_hi:[0,0,0] cbsz:2 blgp:4
	v_mfma_scale_f32_32x32x64_f8f6f4 v[18:33], v[108:113], v[138:141], v[18:33], v89, v88 op_sel:[1,0,0] op_sel_hi:[0,0,0] cbsz:2 blgp:4
	v_mfma_scale_f32_32x32x64_f8f6f4 v[2:17], v[108:113], v[142:145], v[2:17], v89, v88 op_sel:[1,0,0] op_sel_hi:[0,0,0] cbsz:2 blgp:4
	s_setprio 0
	s_barrier
	s_add_i32 s8, s55, 2
	s_and_b32 s8, s8, 6
	ds_read_b128 v[114:117], v77 offset:40960
	ds_read_b128 v[118:121], v77 offset:41472
	ds_read_b128 v[122:125], v77 offset:41984
	ds_read_b128 v[126:129], v77 offset:42496
	ds_read_b64 v[90:91], v75
	ds_read_b64 v[92:93], v75 offset:8
	ds_read_b64 v[94:95], v75 offset:16
	ds_read_b64 v[96:97], v76
	ds_read_b64 v[98:99], v76 offset:8
	ds_read_b64 v[100:101], v76 offset:16
	v_lshl_add_u32 v89, s8, 9, v87
	ds_read_u16 v154, v89
	ds_read_b128 v[130:133], v77 offset:49152
	ds_read_b128 v[134:137], v77 offset:49664
	ds_read_b128 v[138:141], v77 offset:50176
	ds_read_b128 v[142:145], v77 offset:50688
	ds_read_b64 v[102:103], v74
	ds_read_b64 v[104:105], v74 offset:8
	ds_read_b64 v[106:107], v74 offset:16
	s_mov_b32 m0, s38
	ds_read_b64 v[108:109], v73
	ds_read_b64 v[110:111], v73 offset:8
	ds_read_b64 v[112:113], v73 offset:16
	ds_read_u16 v89, v89 offset:512
	global_load_lds_dwordx4 v163, s[72:73]
	s_mov_b32 m0, s39
	s_add_i32 s8, s56, 6
	global_load_lds_dwordx4 v164, s[72:73]
	s_mov_b32 m0, s40
	s_min_u32 s58, s8, 63
	global_load_lds_dwordx4 v170, s[76:77]
	s_mov_b32 m0, s41
	s_lshl_b32 s8, s58, 10
	global_load_lds_dwordx4 v171, s[76:77]
	s_mov_b32 m0, s42
	s_nop 0
	global_load_lds_dwordx4 v172, s[76:77]
	s_add_u32 s82, s80, s8
	s_addc_u32 s83, s81, 0
	s_lshl_b32 s8, s58, 9
	s_and_b32 s8, s8, 0xe00
	s_add_i32 m0, s49, s8
	s_nop 0
	global_load_lds_dword v160, s[82:83]
	s_sleep 3
	s_waitcnt vmcnt(6)
	s_waitcnt lgkmcnt(0)
	s_barrier
	s_setprio 1
	s_waitcnt lgkmcnt(0)
	v_mfma_scale_f32_32x32x64_f8f6f4 v[50:65], v[90:95], v[114:117], v[50:65], v154, v88 op_sel_hi:[0,0,0] cbsz:2 blgp:4
	v_mfma_scale_f32_32x32x64_f8f6f4 v[34:49], v[90:95], v[118:121], v[34:49], v154, v88 op_sel_hi:[0,0,0] cbsz:2 blgp:4
	v_mfma_scale_f32_32x32x64_f8f6f4 v[18:33], v[90:95], v[122:125], v[18:33], v154, v88 op_sel_hi:[0,0,0] cbsz:2 blgp:4
	v_mfma_scale_f32_32x32x64_f8f6f4 v[2:17], v[90:95], v[126:129], v[2:17], v154, v88 op_sel_hi:[0,0,0] cbsz:2 blgp:4
	v_mfma_scale_f32_32x32x64_f8f6f4 v[50:65], v[96:101], v[114:117], v[50:65], v154, v88 op_sel:[1,0,0] op_sel_hi:[0,0,0] cbsz:2 blgp:4
	v_mfma_scale_f32_32x32x64_f8f6f4 v[34:49], v[96:101], v[118:121], v[34:49], v154, v88 op_sel:[1,0,0] op_sel_hi:[0,0,0] cbsz:2 blgp:4
	v_mfma_scale_f32_32x32x64_f8f6f4 v[18:33], v[96:101], v[122:125], v[18:33], v154, v88 op_sel:[1,0,0] op_sel_hi:[0,0,0] cbsz:2 blgp:4
	v_mfma_scale_f32_32x32x64_f8f6f4 v[2:17], v[96:101], v[126:129], v[2:17], v154, v88 op_sel:[1,0,0] op_sel_hi:[0,0,0] cbsz:2 blgp:4
	v_mfma_scale_f32_32x32x64_f8f6f4 v[50:65], v[102:107], v[130:133], v[50:65], v89, v88 op_sel_hi:[0,0,0] cbsz:2 blgp:4
	v_mfma_scale_f32_32x32x64_f8f6f4 v[34:49], v[102:107], v[134:137], v[34:49], v89, v88 op_sel_hi:[0,0,0] cbsz:2 blgp:4
	v_mfma_scale_f32_32x32x64_f8f6f4 v[18:33], v[102:107], v[138:141], v[18:33], v89, v88 op_sel_hi:[0,0,0] cbsz:2 blgp:4
	v_mfma_scale_f32_32x32x64_f8f6f4 v[2:17], v[102:107], v[142:145], v[2:17], v89, v88 op_sel_hi:[0,0,0] cbsz:2 blgp:4
	v_mfma_scale_f32_32x32x64_f8f6f4 v[50:65], v[108:113], v[130:133], v[50:65], v89, v88 op_sel:[1,0,0] op_sel_hi:[0,0,0] cbsz:2 blgp:4
	v_mfma_scale_f32_32x32x64_f8f6f4 v[34:49], v[108:113], v[134:137], v[34:49], v89, v88 op_sel:[1,0,0] op_sel_hi:[0,0,0] cbsz:2 blgp:4
	v_mfma_scale_f32_32x32x64_f8f6f4 v[18:33], v[108:113], v[138:141], v[18:33], v89, v88 op_sel:[1,0,0] op_sel_hi:[0,0,0] cbsz:2 blgp:4
	v_mfma_scale_f32_32x32x64_f8f6f4 v[2:17], v[108:113], v[142:145], v[2:17], v89, v88 op_sel:[1,0,0] op_sel_hi:[0,0,0] cbsz:2 blgp:4
	s_setprio 0
	s_barrier
	s_and_b32 s8, s57, 6
	ds_read_b128 v[114:117], v86
	ds_read_b128 v[118:121], v86 offset:512
	ds_read_b128 v[122:125], v86 offset:1024
	ds_read_b128 v[126:129], v86 offset:1536
	ds_read_b64 v[90:91], v82
	ds_read_b64 v[92:93], v82 offset:8
	ds_read_b64 v[94:95], v82 offset:16
	ds_read_b64 v[96:97], v83
	ds_read_b64 v[98:99], v83 offset:8
	ds_read_b64 v[100:101], v83 offset:16
	v_lshl_add_u32 v89, s8, 9, v87
	ds_read_u16 v154, v89
	ds_read_b128 v[130:133], v86 offset:8192
	ds_read_b128 v[134:137], v86 offset:8704
	ds_read_b128 v[138:141], v86 offset:9216
	ds_read_b128 v[142:145], v86 offset:9728
	ds_read_b64 v[102:103], v84
	ds_read_b64 v[104:105], v84 offset:8
	ds_read_b64 v[106:107], v84 offset:16
	s_mov_b32 m0, s43
	ds_read_b64 v[108:109], v85
	ds_read_b64 v[110:111], v85 offset:8
	ds_read_b64 v[112:113], v85 offset:16
	ds_read_u16 v89, v89 offset:512
	global_load_lds_dwordx4 v165, s[72:73]
	s_mov_b32 m0, s44
	s_nop 0
	global_load_lds_dwordx4 v166, s[72:73]
	s_mov_b32 m0, s45
	s_add_i32 s56, s56, 8
	global_load_lds_dwordx4 v173, s[76:77]
	s_mov_b32 m0, s46
	s_min_u32 s56, s56, 63
	global_load_lds_dwordx4 v174, s[76:77]
	s_mov_b32 m0, s47
	s_lshl_b32 s8, s56, 10
	global_load_lds_dwordx4 v175, s[76:77]
	s_add_u32 s82, s80, s8
	s_addc_u32 s83, s81, 0
	s_lshl_b32 s8, s56, 9
	s_and_b32 s8, s8, 0xe00
	s_add_i32 m0, s49, s8
	s_nop 0
	global_load_lds_dword v160, s[82:83]
	s_sleep 3
	s_waitcnt vmcnt(6)
	s_waitcnt lgkmcnt(0)
	s_barrier
	s_setprio 1
	s_waitcnt lgkmcnt(0)
	v_mfma_scale_f32_32x32x64_f8f6f4 v[50:65], v[90:95], v[114:117], v[50:65], v154, v88 op_sel_hi:[0,0,0] cbsz:2 blgp:4
	v_mfma_scale_f32_32x32x64_f8f6f4 v[34:49], v[90:95], v[118:121], v[34:49], v154, v88 op_sel_hi:[0,0,0] cbsz:2 blgp:4
	v_mfma_scale_f32_32x32x64_f8f6f4 v[18:33], v[90:95], v[122:125], v[18:33], v154, v88 op_sel_hi:[0,0,0] cbsz:2 blgp:4
	v_mfma_scale_f32_32x32x64_f8f6f4 v[2:17], v[90:95], v[126:129], v[2:17], v154, v88 op_sel_hi:[0,0,0] cbsz:2 blgp:4
	v_mfma_scale_f32_32x32x64_f8f6f4 v[50:65], v[96:101], v[114:117], v[50:65], v154, v88 op_sel:[1,0,0] op_sel_hi:[0,0,0] cbsz:2 blgp:4
	v_mfma_scale_f32_32x32x64_f8f6f4 v[34:49], v[96:101], v[118:121], v[34:49], v154, v88 op_sel:[1,0,0] op_sel_hi:[0,0,0] cbsz:2 blgp:4
	v_mfma_scale_f32_32x32x64_f8f6f4 v[18:33], v[96:101], v[122:125], v[18:33], v154, v88 op_sel:[1,0,0] op_sel_hi:[0,0,0] cbsz:2 blgp:4
	v_mfma_scale_f32_32x32x64_f8f6f4 v[2:17], v[96:101], v[126:129], v[2:17], v154, v88 op_sel:[1,0,0] op_sel_hi:[0,0,0] cbsz:2 blgp:4
	v_mfma_scale_f32_32x32x64_f8f6f4 v[50:65], v[102:107], v[130:133], v[50:65], v89, v88 op_sel_hi:[0,0,0] cbsz:2 blgp:4
	v_mfma_scale_f32_32x32x64_f8f6f4 v[34:49], v[102:107], v[134:137], v[34:49], v89, v88 op_sel_hi:[0,0,0] cbsz:2 blgp:4
	v_mfma_scale_f32_32x32x64_f8f6f4 v[18:33], v[102:107], v[138:141], v[18:33], v89, v88 op_sel_hi:[0,0,0] cbsz:2 blgp:4
	v_mfma_scale_f32_32x32x64_f8f6f4 v[2:17], v[102:107], v[142:145], v[2:17], v89, v88 op_sel_hi:[0,0,0] cbsz:2 blgp:4
	v_mfma_scale_f32_32x32x64_f8f6f4 v[50:65], v[108:113], v[130:133], v[50:65], v89, v88 op_sel:[1,0,0] op_sel_hi:[0,0,0] cbsz:2 blgp:4
	v_mfma_scale_f32_32x32x64_f8f6f4 v[34:49], v[108:113], v[134:137], v[34:49], v89, v88 op_sel:[1,0,0] op_sel_hi:[0,0,0] cbsz:2 blgp:4
	v_mfma_scale_f32_32x32x64_f8f6f4 v[18:33], v[108:113], v[138:141], v[18:33], v89, v88 op_sel:[1,0,0] op_sel_hi:[0,0,0] cbsz:2 blgp:4
	v_mfma_scale_f32_32x32x64_f8f6f4 v[2:17], v[108:113], v[142:145], v[2:17], v89, v88 op_sel:[1,0,0] op_sel_hi:[0,0,0] cbsz:2 blgp:4
	s_setprio 0
	s_barrier
	s_add_i32 s48, s48, 3
	s_add_i32 s55, s55, 6
	s_add_u32 s72, s72, 0xc000
	s_addc_u32 s73, s73, 0
	s_add_u32 s76, s76, 0x24000
	s_addc_u32 s77, s77, 0
	s_cmp_lt_u32 s48, 27
	s_cbranch_scc1 .LBB1_3
	ds_read_b128 v[66:69], v77
	ds_read_b128 v[106:109], v77 offset:512
	ds_read_b128 v[110:113], v77 offset:1024
	ds_read_b128 v[114:117], v77 offset:1536
	ds_read_b64 v[82:83], v78
	ds_read_b64 v[84:85], v78 offset:8
	ds_read_b64 v[86:87], v78 offset:16
	ds_read_b64 v[88:89], v81
	ds_read_b64 v[90:91], v81 offset:8
	ds_read_b64 v[92:93], v81 offset:16
	v_add_u32_e32 v0, 0x1e800, v72
	ds_read_u16 v0, v0
	ds_read_b128 v[118:121], v77 offset:8192
	ds_read_b128 v[122:125], v77 offset:8704
	ds_read_b128 v[126:129], v77 offset:9216
	ds_read_b128 v[130:133], v77 offset:9728
	ds_read_b64 v[94:95], v80
	ds_read_b64 v[96:97], v80 offset:8
	ds_read_b64 v[98:99], v80 offset:16
	ds_read_b64 v[100:101], v79
	ds_read_b64 v[102:103], v79 offset:8
	ds_read_b64 v[104:105], v79 offset:16
	v_add_u32_e32 v1, 0x1ea00, v72
	ds_read_u16 v1, v1
	s_waitcnt vmcnt(0)
	s_waitcnt lgkmcnt(0)
	s_barrier
	s_setprio 1
	v_mov_b32_e32 v134, 0x7f7f7f7f
	s_waitcnt lgkmcnt(0)
	s_nop 0
	v_mfma_scale_f32_32x32x64_f8f6f4 v[50:65], v[82:87], v[66:69], v[50:65], v0, v134 op_sel_hi:[0,0,0] cbsz:2 blgp:4
	v_mfma_scale_f32_32x32x64_f8f6f4 v[34:49], v[82:87], v[106:109], v[34:49], v0, v134 op_sel_hi:[0,0,0] cbsz:2 blgp:4
	v_mfma_scale_f32_32x32x64_f8f6f4 v[18:33], v[82:87], v[110:113], v[18:33], v0, v134 op_sel_hi:[0,0,0] cbsz:2 blgp:4
	v_mfma_scale_f32_32x32x64_f8f6f4 v[2:17], v[82:87], v[114:117], v[2:17], v0, v134 op_sel_hi:[0,0,0] cbsz:2 blgp:4
	v_mfma_scale_f32_32x32x64_f8f6f4 v[50:65], v[88:93], v[66:69], v[50:65], v0, v134 op_sel:[1,0,0] op_sel_hi:[0,0,0] cbsz:2 blgp:4
	v_mfma_scale_f32_32x32x64_f8f6f4 v[34:49], v[88:93], v[106:109], v[34:49], v0, v134 op_sel:[1,0,0] op_sel_hi:[0,0,0] cbsz:2 blgp:4
	v_mfma_scale_f32_32x32x64_f8f6f4 v[18:33], v[88:93], v[110:113], v[18:33], v0, v134 op_sel:[1,0,0] op_sel_hi:[0,0,0] cbsz:2 blgp:4
	v_mfma_scale_f32_32x32x64_f8f6f4 v[2:17], v[88:93], v[114:117], v[2:17], v0, v134 op_sel:[1,0,0] op_sel_hi:[0,0,0] cbsz:2 blgp:4
	v_lshrrev_b32_e32 v0, 8, v1
	v_mfma_scale_f32_32x32x64_f8f6f4 v[50:65], v[94:99], v[118:121], v[50:65], v1, v134 op_sel_hi:[0,0,0] cbsz:2 blgp:4
	v_mfma_scale_f32_32x32x64_f8f6f4 v[34:49], v[94:99], v[122:125], v[34:49], v1, v134 op_sel_hi:[0,0,0] cbsz:2 blgp:4
	v_mfma_scale_f32_32x32x64_f8f6f4 v[18:33], v[94:99], v[126:129], v[18:33], v1, v134 op_sel_hi:[0,0,0] cbsz:2 blgp:4
	v_mfma_scale_f32_32x32x64_f8f6f4 v[2:17], v[94:99], v[130:133], v[2:17], v1, v134 op_sel_hi:[0,0,0] cbsz:2 blgp:4
	v_mfma_scale_f32_32x32x64_f8f6f4 v[50:65], v[100:105], v[118:121], v[50:65], v0, v134 op_sel_hi:[0,0,0] cbsz:2 blgp:4
	v_mfma_scale_f32_32x32x64_f8f6f4 v[34:49], v[100:105], v[122:125], v[34:49], v0, v134 op_sel_hi:[0,0,0] cbsz:2 blgp:4
	v_mfma_scale_f32_32x32x64_f8f6f4 v[18:33], v[100:105], v[126:129], v[18:33], v0, v134 op_sel_hi:[0,0,0] cbsz:2 blgp:4
	v_mfma_scale_f32_32x32x64_f8f6f4 v[2:17], v[100:105], v[130:133], v[2:17], v0, v134 op_sel_hi:[0,0,0] cbsz:2 blgp:4
	s_setprio 0
	s_barrier
	ds_read_b128 v[66:69], v77 offset:40960
	ds_read_b128 v[102:105], v77 offset:41472
	ds_read_b128 v[106:109], v77 offset:41984
	ds_read_b128 v[110:113], v77 offset:42496
	ds_read_b64 v[78:79], v75
	ds_read_b64 v[80:81], v75 offset:8
	ds_read_b64 v[82:83], v75 offset:16
	ds_read_b64 v[84:85], v76
	ds_read_b64 v[86:87], v76 offset:8
	ds_read_b64 v[88:89], v76 offset:16
	v_add_u32_e32 v0, 0x1ec00, v72
	ds_read_u16 v0, v0
	ds_read_b128 v[114:117], v77 offset:49152
	ds_read_b128 v[118:121], v77 offset:49664
	ds_read_b128 v[122:125], v77 offset:50176
	ds_read_b128 v[126:129], v77 offset:50688
	ds_read_b64 v[90:91], v74
	ds_read_b64 v[92:93], v74 offset:8
	ds_read_b64 v[94:95], v74 offset:16
	ds_read_b64 v[96:97], v73
	ds_read_b64 v[98:99], v73 offset:8
	ds_read_b64 v[100:101], v73 offset:16
	v_add_u32_e32 v1, 0x1ee00, v72
	ds_read_u16 v1, v1
	s_waitcnt vmcnt(0)
	s_waitcnt lgkmcnt(0)
	s_barrier
	s_setprio 1
	s_waitcnt lgkmcnt(0)
	v_mfma_scale_f32_32x32x64_f8f6f4 v[50:65], v[78:83], v[66:69], v[50:65], v0, v134 op_sel_hi:[0,0,0] cbsz:2 blgp:4
	v_mfma_scale_f32_32x32x64_f8f6f4 v[34:49], v[78:83], v[102:105], v[34:49], v0, v134 op_sel_hi:[0,0,0] cbsz:2 blgp:4
	v_mfma_scale_f32_32x32x64_f8f6f4 v[18:33], v[78:83], v[106:109], v[18:33], v0, v134 op_sel_hi:[0,0,0] cbsz:2 blgp:4
	v_mfma_scale_f32_32x32x64_f8f6f4 v[2:17], v[78:83], v[110:113], v[2:17], v0, v134 op_sel_hi:[0,0,0] cbsz:2 blgp:4
	v_mfma_scale_f32_32x32x64_f8f6f4 v[50:65], v[84:89], v[66:69], v[50:65], v0, v134 op_sel:[1,0,0] op_sel_hi:[0,0,0] cbsz:2 blgp:4
	v_mfma_scale_f32_32x32x64_f8f6f4 v[34:49], v[84:89], v[102:105], v[34:49], v0, v134 op_sel:[1,0,0] op_sel_hi:[0,0,0] cbsz:2 blgp:4
	v_mfma_scale_f32_32x32x64_f8f6f4 v[18:33], v[84:89], v[106:109], v[18:33], v0, v134 op_sel:[1,0,0] op_sel_hi:[0,0,0] cbsz:2 blgp:4
	v_mfma_scale_f32_32x32x64_f8f6f4 v[2:17], v[84:89], v[110:113], v[2:17], v0, v134 op_sel:[1,0,0] op_sel_hi:[0,0,0] cbsz:2 blgp:4
	v_lshrrev_b32_e32 v0, 8, v1
	v_mfma_scale_f32_32x32x64_f8f6f4 v[50:65], v[90:95], v[114:117], v[50:65], v1, v134 op_sel_hi:[0,0,0] cbsz:2 blgp:4
	v_mfma_scale_f32_32x32x64_f8f6f4 v[34:49], v[90:95], v[118:121], v[34:49], v1, v134 op_sel_hi:[0,0,0] cbsz:2 blgp:4
	v_mfma_scale_f32_32x32x64_f8f6f4 v[18:33], v[90:95], v[122:125], v[18:33], v1, v134 op_sel_hi:[0,0,0] cbsz:2 blgp:4
	v_mfma_scale_f32_32x32x64_f8f6f4 v[2:17], v[90:95], v[126:129], v[2:17], v1, v134 op_sel_hi:[0,0,0] cbsz:2 blgp:4
	v_mfma_scale_f32_32x32x64_f8f6f4 v[50:65], v[96:101], v[114:117], v[50:65], v0, v134 op_sel_hi:[0,0,0] cbsz:2 blgp:4
	v_mfma_scale_f32_32x32x64_f8f6f4 v[34:49], v[96:101], v[118:121], v[34:49], v0, v134 op_sel_hi:[0,0,0] cbsz:2 blgp:4
	v_mfma_scale_f32_32x32x64_f8f6f4 v[18:33], v[96:101], v[122:125], v[18:33], v0, v134 op_sel_hi:[0,0,0] cbsz:2 blgp:4
	v_mfma_scale_f32_32x32x64_f8f6f4 v[2:17], v[96:101], v[126:129], v[2:17], v0, v134 op_sel_hi:[0,0,0] cbsz:2 blgp:4
	s_setprio 0
	s_barrier
	s_cmpk_gt_u32 s33, 0xff
	s_cbranch_scc1 .LBB1_6
	s_barrier
